# v049 + route phase: router-weight staging issues all 32 loads before the LDS writes; second row of each two-row pass fetched together with the first (one exposed round trip per pass less)
# speedup vs baseline: 1.0052x; 1.0052x over previous
.Lstage_route:
	v_lshlrev_b32_e32 v160, 2, v0
	s_mov_b64 s[98:99], s[48:49]
	global_load_dword v164, v160, s[98:99]
	global_load_dword v165, v160, s[98:99] offset:2048
	s_add_u32 s98, s98, 0x1000
	s_addc_u32 s99, s99, 0
	global_load_dword v166, v160, s[98:99]
	global_load_dword v167, v160, s[98:99] offset:2048
	s_add_u32 s98, s98, 0x1000
	s_addc_u32 s99, s99, 0
	global_load_dword v168, v160, s[98:99]
	global_load_dword v169, v160, s[98:99] offset:2048
	s_add_u32 s98, s98, 0x1000
	s_addc_u32 s99, s99, 0
	global_load_dword v170, v160, s[98:99]
	global_load_dword v171, v160, s[98:99] offset:2048
	s_add_u32 s98, s98, 0x1000
	s_addc_u32 s99, s99, 0
	global_load_dword v172, v160, s[98:99]
	global_load_dword v173, v160, s[98:99] offset:2048
	s_add_u32 s98, s98, 0x1000
	s_addc_u32 s99, s99, 0
	global_load_dword v174, v160, s[98:99]
	global_load_dword v175, v160, s[98:99] offset:2048
	s_add_u32 s98, s98, 0x1000
	s_addc_u32 s99, s99, 0
	global_load_dword v176, v160, s[98:99]
	global_load_dword v177, v160, s[98:99] offset:2048
	s_add_u32 s98, s98, 0x1000
	s_addc_u32 s99, s99, 0
	global_load_dword v178, v160, s[98:99]
	global_load_dword v179, v160, s[98:99] offset:2048
	s_add_u32 s98, s98, 0x1000
	s_addc_u32 s99, s99, 0
	global_load_dword v180, v160, s[98:99]
	global_load_dword v181, v160, s[98:99] offset:2048
	s_add_u32 s98, s98, 0x1000
	s_addc_u32 s99, s99, 0
	global_load_dword v182, v160, s[98:99]
	global_load_dword v183, v160, s[98:99] offset:2048
	s_add_u32 s98, s98, 0x1000
	s_addc_u32 s99, s99, 0
	global_load_dword v184, v160, s[98:99]
	global_load_dword v185, v160, s[98:99] offset:2048
	s_add_u32 s98, s98, 0x1000
	s_addc_u32 s99, s99, 0
	global_load_dword v186, v160, s[98:99]
	global_load_dword v187, v160, s[98:99] offset:2048
	s_add_u32 s98, s98, 0x1000
	s_addc_u32 s99, s99, 0
	global_load_dword v188, v160, s[98:99]
	global_load_dword v189, v160, s[98:99] offset:2048
	s_add_u32 s98, s98, 0x1000
	s_addc_u32 s99, s99, 0
	global_load_dword v190, v160, s[98:99]
	global_load_dword v191, v160, s[98:99] offset:2048
	s_add_u32 s98, s98, 0x1000
	s_addc_u32 s99, s99, 0
	global_load_dword v192, v160, s[98:99]
	global_load_dword v193, v160, s[98:99] offset:2048
	s_add_u32 s98, s98, 0x1000
	s_addc_u32 s99, s99, 0
	global_load_dword v194, v160, s[98:99]
	global_load_dword v195, v160, s[98:99] offset:2048
	v_and_b32_e32 v161, 7, v0
	v_lshrrev_b32_e32 v162, 3, v0
	v_lshlrev_b32_e32 v161, 13, v161
	v_lshl_or_b32 v161, v162, 2, v161
	s_waitcnt vmcnt(31)
	ds_write_b32 v161, v164 offset:0
	s_waitcnt vmcnt(30)
	ds_write_b32 v161, v165 offset:256
	s_waitcnt vmcnt(29)
	ds_write_b32 v161, v166 offset:512
	s_waitcnt vmcnt(28)
	ds_write_b32 v161, v167 offset:768
	s_waitcnt vmcnt(27)
	ds_write_b32 v161, v168 offset:1024
	s_waitcnt vmcnt(26)
	ds_write_b32 v161, v169 offset:1280
	s_waitcnt vmcnt(25)
	ds_write_b32 v161, v170 offset:1536
	s_waitcnt vmcnt(24)
	ds_write_b32 v161, v171 offset:1792
	s_waitcnt vmcnt(23)
	ds_write_b32 v161, v172 offset:2048
	s_waitcnt vmcnt(22)
	ds_write_b32 v161, v173 offset:2304
	s_waitcnt vmcnt(21)
	ds_write_b32 v161, v174 offset:2560
	s_waitcnt vmcnt(20)
	ds_write_b32 v161, v175 offset:2816
	s_waitcnt vmcnt(19)
	ds_write_b32 v161, v176 offset:3072
	s_waitcnt vmcnt(18)
	ds_write_b32 v161, v177 offset:3328
	s_waitcnt vmcnt(17)
	ds_write_b32 v161, v178 offset:3584
	s_waitcnt vmcnt(16)
	ds_write_b32 v161, v179 offset:3840
	s_waitcnt vmcnt(15)
	ds_write_b32 v161, v180 offset:4096
	s_waitcnt vmcnt(14)
	ds_write_b32 v161, v181 offset:4352
	s_waitcnt vmcnt(13)
	ds_write_b32 v161, v182 offset:4608
	s_waitcnt vmcnt(12)
	ds_write_b32 v161, v183 offset:4864
	s_waitcnt vmcnt(11)
	ds_write_b32 v161, v184 offset:5120
	s_waitcnt vmcnt(10)
	ds_write_b32 v161, v185 offset:5376
	s_waitcnt vmcnt(9)
	ds_write_b32 v161, v186 offset:5632
	s_waitcnt vmcnt(8)
	ds_write_b32 v161, v187 offset:5888
	s_waitcnt vmcnt(7)
	ds_write_b32 v161, v188 offset:6144
	s_waitcnt vmcnt(6)
	ds_write_b32 v161, v189 offset:6400
	s_waitcnt vmcnt(5)
	ds_write_b32 v161, v190 offset:6656
	s_waitcnt vmcnt(4)
	ds_write_b32 v161, v191 offset:6912
	s_waitcnt vmcnt(3)
	ds_write_b32 v161, v192 offset:7168
	s_waitcnt vmcnt(2)
	ds_write_b32 v161, v193 offset:7424
	s_waitcnt vmcnt(1)
	ds_write_b32 v161, v194 offset:7680
	s_waitcnt vmcnt(0)
	ds_write_b32 v161, v195 offset:7936
	s_or_b64 exec, exec, s[0:1]
	v_mov_b32_e32 v1, 0
	v_cmp_ne_u32_e64 s[2:3], 0, 0
	s_and_saveexec_b64 s[0:1], s[2:3]
	s_cbranch_execz .LBB0_1334
	s_mov_b64 s[4:5], 0
	v_mov_b32_e32 v5, 0

.LBB0_1344:
	s_add_i32 s2, s50, s58
	s_add_i32 s12, s2, 2
	s_ashr_i32 s13, s12, 31
	s_lshl_b64 s[14:15], s[12:13], 13
	s_add_i32 s98, s2, 3
	s_ashr_i32 s99, s98, 31
	s_lshl_b64 s[98:99], s[98:99], 13
	v_lshl_add_u64 v[160:161], v[54:55], 0, s[98:99]
	v_lshl_add_u64 v[34:35], v[54:55], 0, s[14:15]
	global_load_dwordx4 v[56:59], v[34:35], off
	global_load_dwordx4 v[60:63], v[34:35], off offset:1024
	global_load_dwordx4 v[64:67], v[34:35], off offset:2048
	global_load_dwordx4 v[68:71], v[34:35], off offset:3072
	v_add_co_u32_e32 v42, vcc, s3, v34
	s_lshl_b64 s[12:13], s[12:13], 11
	s_nop 0
	v_addc_co_u32_e32 v43, vcc, 0, v35, vcc
	global_load_dwordx4 v[38:41], v[42:43], off
	global_load_dwordx4 v[46:49], v[42:43], off offset:1024
	global_load_dwordx4 v[34:37], v[42:43], off offset:3072
	s_nop 0
	global_load_dwordx4 v[42:45], v[42:43], off offset:2048
	global_load_dwordx4 v[164:167], v[160:161], off
	global_load_dwordx4 v[168:171], v[160:161], off offset:1024
	global_load_dwordx4 v[172:175], v[160:161], off offset:2048
	global_load_dwordx4 v[176:179], v[160:161], off offset:3072
	v_add_co_u32_e32 v162, vcc, s3, v160
	s_nop 1
	v_addc_co_u32_e32 v163, vcc, 0, v161, vcc
	s_nop 0
	global_load_dwordx4 v[180:183], v[162:163], off
	global_load_dwordx4 v[184:187], v[162:163], off offset:1024
	global_load_dwordx4 v[188:191], v[162:163], off offset:2048
	global_load_dwordx4 v[192:195], v[162:163], off offset:3072
	v_cmp_lt_i32_e32 vcc, v108, v107
	s_waitcnt vmcnt(15)
	v_mov_b32_e32 v74, v57
	v_cndmask_b32_e32 v72, v106, v108, vcc
	s_waitcnt vmcnt(14)
	v_mov_b32_e32 v75, v61
	v_mov_b32_e32 v78, v59
	v_mov_b32_e32 v79, v63
	v_lshlrev_b32_e32 v118, 2, v72
	v_mov_b32_e32 v72, v56
	v_mov_b32_e32 v73, v60
	v_mov_b32_e32 v76, v58
	v_mov_b32_e32 v77, v62
	s_waitcnt vmcnt(13)
	v_pk_mul_f32 v[80:81], v[66:67], v[66:67]
	v_pk_mul_f32 v[82:83], v[64:65], v[64:65]
	v_pk_mul_f32 v[74:75], v[74:75], v[74:75]
	v_pk_mul_f32 v[78:79], v[78:79], v[78:79]
	v_pk_mov_b32 v[88:89], v[82:83], v[80:81] op_sel:[1,0]
	v_mov_b32_e32 v83, v81
	v_pk_fma_f32 v[72:73], v[72:73], v[72:73], v[74:75]
	v_pk_fma_f32 v[74:75], v[76:77], v[76:77], v[78:79]
	s_waitcnt vmcnt(12)
	v_mul_f32_e32 v84, v69, v69
	v_mul_f32_e32 v86, v71, v71
	v_pk_add_f32 v[76:77], v[88:89], v[82:83]
	v_pk_add_f32 v[72:73], v[72:73], v[74:75]
	s_waitcnt vmcnt(11)
	v_mul_f32_e32 v93, v38, v38
	v_mul_f32_e32 v95, v39, v39
	v_mul_f32_e32 v96, v40, v40
	v_mul_f32_e32 v97, v41, v41
	v_pk_fma_f32 v[80:81], v[68:69], v[68:69], v[84:85] op_sel_hi:[1,1,0]
	v_pk_fma_f32 v[84:85], v[70:71], v[70:71], v[86:87] op_sel_hi:[1,1,0]
	v_pk_add_f32 v[74:75], v[76:77], v[76:77] op_sel:[0,1] op_sel_hi:[1,0]
	v_pk_add_f32 v[72:73], v[72:73], v[72:73] op_sel:[0,1] op_sel_hi:[1,0]
	s_waitcnt vmcnt(10)
	v_pk_mul_f32 v[86:87], v[48:49], v[48:49]
	v_pk_mul_f32 v[90:91], v[46:47], v[46:47]
	v_mov_b32_e32 v81, v96
	v_mov_b32_e32 v85, v97
	v_mov_b32_e32 v75, v95
	v_mov_b32_e32 v73, v93
	v_pk_mov_b32 v[78:79], v[90:91], v[86:87] op_sel:[1,0]
	v_mov_b32_e32 v91, v87
	v_pk_add_f32 v[76:77], v[80:81], v[84:85]
	v_pk_add_f32 v[72:73], v[72:73], v[74:75]
	s_waitcnt vmcnt(8)
	v_mul_f32_e32 v92, v43, v43
	v_mul_f32_e32 v94, v45, v45
	v_pk_add_f32 v[78:79], v[78:79], v[90:91]
	v_pk_add_f32 v[72:73], v[72:73], v[76:77]
	v_mul_f32_e32 v98, v34, v34
	v_mul_f32_e32 v99, v35, v35
	v_mul_f32_e32 v100, v36, v36
	v_mul_f32_e32 v101, v37, v37
	v_pk_fma_f32 v[82:83], v[42:43], v[42:43], v[92:93] op_sel_hi:[1,1,0]
	v_pk_fma_f32 v[86:87], v[44:45], v[44:45], v[94:95] op_sel_hi:[1,1,0]
	v_pk_add_f32 v[78:79], v[78:79], v[78:79] op_sel:[0,1] op_sel_hi:[1,0]
	v_pk_add_f32 v[72:73], v[72:73], v[72:73] op_sel:[0,1] op_sel_hi:[1,0]
	v_mov_b32_e32 v83, v100
	v_mov_b32_e32 v87, v101
	v_mov_b32_e32 v79, v99
	v_mov_b32_e32 v73, v98
	v_pk_add_f32 v[80:81], v[82:83], v[86:87]
	v_pk_add_f32 v[72:73], v[72:73], v[78:79]
	v_cmp_lt_i32_e32 vcc, v109, v107
	v_pk_add_f32 v[72:73], v[72:73], v[80:81]
	v_mov_b32_e32 v79, 0
	v_add_f32_e32 v72, v72, v73
	ds_bpermute_b32 v73, v118, v72
	v_cndmask_b32_e32 v74, v106, v109, vcc
	v_lshlrev_b32_e32 v119, 2, v74
	v_cmp_lt_i32_e32 vcc, v110, v107
	v_mov_b32_e32 v85, 0
	s_waitcnt lgkmcnt(0)
	v_add_f32_e32 v72, v72, v73
	ds_bpermute_b32 v73, v119, v72
	v_cndmask_b32_e32 v74, v106, v110, vcc
	v_lshlrev_b32_e32 v120, 2, v74
	v_cmp_lt_i32_e32 vcc, v111, v107
	v_mov_b32_e32 v84, 0
	s_waitcnt lgkmcnt(0)
	v_add_f32_e32 v72, v72, v73
	ds_bpermute_b32 v73, v120, v72
	v_cndmask_b32_e32 v74, v106, v111, vcc
	v_lshlrev_b32_e32 v121, 2, v74
	v_cmp_lt_i32_e32 vcc, v112, v107
	v_lshl_add_u64 v[76:77], v[52:53], 0, s[12:13]
	s_waitcnt lgkmcnt(0)
	v_add_f32_e32 v72, v72, v73
	ds_bpermute_b32 v73, v121, v72
	v_cndmask_b32_e32 v74, v106, v112, vcc
	v_lshlrev_b32_e32 v122, 2, v74
	v_cmp_lt_i32_e32 vcc, v113, v107
	s_add_i32 s12, s2, 3
	s_waitcnt lgkmcnt(0)
	v_add_f32_e32 v72, v72, v73
	ds_bpermute_b32 v73, v122, v72
	v_cndmask_b32_e32 v74, v106, v113, vcc
	v_lshlrev_b32_e32 v123, 2, v74
	s_ashr_i32 s13, s12, 31
	s_lshl_b64 s[14:15], s[12:13], 13
	s_waitcnt lgkmcnt(0)
	v_add_f32_e32 v72, v72, v73
	ds_bpermute_b32 v73, v123, v72
	s_lshl_b64 s[12:13], s[12:13], 11
	s_waitcnt lgkmcnt(0)
	v_add_f32_e32 v72, v72, v73
	v_fmamk_f32 v72, v72, 0x3a000000, v114
	v_mul_f32_e32 v73, 0x4b800000, v72
	v_cmp_gt_f32_e32 vcc, s52, v72
	s_nop 1
	v_cndmask_b32_e32 v72, v72, v73, vcc
	v_rsq_f32_e32 v72, v72
	s_nop 0
	v_mul_f32_e32 v73, 0x45800000, v72
	v_cndmask_b32_e32 v78, v72, v73, vcc
	v_pk_mul_f32 v[56:57], v[56:57], v[78:79] op_sel_hi:[1,0]
	v_pk_mul_f32 v[64:65], v[64:65], v[78:79] op_sel_hi:[1,0]
	v_pk_mul_f32 v[58:59], v[58:59], v[78:79] op_sel_hi:[1,0]
	v_pk_mul_f32 v[74:75], v[2:3], v[56:57]
	v_pk_mul_f32 v[64:65], v[10:11], v[64:65]
	v_pk_mul_f32 v[72:73], v[4:5], v[58:59]
	v_med3_f32 v58, v74, s53, v115
	v_med3_f32 v59, v75, s53, v115
	v_med3_f32 v86, v64, s53, v115
	v_med3_f32 v87, v65, s53, v115
	v_pk_mul_f32 v[60:61], v[60:61], v[78:79] op_sel_hi:[1,0]
	v_pk_mul_f32 v[62:63], v[62:63], v[78:79] op_sel_hi:[1,0]
	v_pk_mul_f32 v[66:67], v[66:67], v[78:79] op_sel_hi:[1,0]
	v_pk_mul_f32 v[80:81], v[68:69], v[78:79] op_sel_hi:[1,0]
	v_pk_mul_f32 v[82:83], v[70:71], v[78:79] op_sel_hi:[1,0]
	v_cvt_pk_fp8_f32 v79, v58, v59
	v_cvt_pk_fp8_f32 v85, v86, v87
	v_pk_mul_f32 v[70:71], v[6:7], v[60:61]
	v_pk_mul_f32 v[60:61], v[12:13], v[66:67]
	v_med3_f32 v66, v70, s53, v115
	v_med3_f32 v67, v71, s53, v115
	v_pk_mul_f32 v[68:69], v[8:9], v[62:63]
	v_pk_mul_f32 v[56:57], v[14:15], v[80:81]
	v_med3_f32 v62, v72, s53, v115
	v_med3_f32 v63, v73, s53, v115
	v_med3_f32 v88, v60, s53, v115
	v_cvt_pk_fp8_f32 v84, v66, v67
	v_med3_f32 v58, v61, s53, v115
	v_cvt_pk_fp8_f32 v79, v62, v63 op_sel:[0,0,1]
	v_cvt_pk_fp8_f32 v85, v88, v58 op_sel:[0,0,1]
	v_med3_f32 v58, v56, s53, v115
	v_med3_f32 v59, v57, s53, v115
	v_cvt_pk_fp8_f32 v62, v58, v59
	v_med3_f32 v80, v68, s53, v115
	v_med3_f32 v81, v69, s53, v115
	v_cvt_pk_fp8_f32 v84, v80, v81 op_sel:[0,0,1]
	v_pk_mul_f32 v[66:67], v[16:17], v[82:83]
	v_pk_mul_f32 v[38:39], v[38:39], v[78:79] op_sel_hi:[1,0]
	v_med3_f32 v58, v66, s53, v115
	v_med3_f32 v59, v67, s53, v115
	v_cvt_pk_fp8_f32 v62, v58, v59 op_sel:[0,0,1]
	v_pk_mul_f32 v[58:59], v[18:19], v[38:39]
	global_store_dword v[76:77], v79, off
	global_store_dword v[76:77], v84, off offset:256
	global_store_dword v[76:77], v85, off offset:512
	global_store_dword v[76:77], v62, off offset:768
	v_pk_mul_f32 v[40:41], v[40:41], v[78:79] op_sel_hi:[1,0]
	v_med3_f32 v38, v58, s53, v115
	v_med3_f32 v39, v59, s53, v115
	v_cvt_pk_fp8_f32 v79, v38, v39
	v_pk_mul_f32 v[62:63], v[20:21], v[40:41]
	v_med3_f32 v38, v62, s53, v115
	v_med3_f32 v39, v63, s53, v115
	v_cvt_pk_fp8_f32 v79, v38, v39 op_sel:[0,0,1]
	v_lshl_add_u64 v[88:89], v[54:55], 0, s[14:15]
	v_add_co_u32_e32 v92, vcc, s3, v88
	v_pk_mul_f32 v[38:39], v[46:47], v[78:79] op_sel_hi:[1,0]
	v_pk_mul_f32 v[40:41], v[48:49], v[78:79] op_sel_hi:[1,0]
	v_pk_mul_f32 v[46:47], v[22:23], v[38:39]
	v_pk_mul_f32 v[48:49], v[24:25], v[40:41]
	v_med3_f32 v38, v46, s53, v115
	v_med3_f32 v39, v47, s53, v115
	v_cvt_pk_fp8_f32 v80, v38, v39
	v_med3_f32 v38, v48, s53, v115
	v_med3_f32 v39, v49, s53, v115
	v_pk_mul_f32 v[40:41], v[44:45], v[78:79] op_sel_hi:[1,0]
	v_cvt_pk_fp8_f32 v80, v38, v39 op_sel:[0,0,1]
	v_pk_mul_f32 v[38:39], v[42:43], v[78:79] op_sel_hi:[1,0]
	v_pk_mul_f32 v[38:39], v[26:27], v[38:39]
	v_pk_mul_f32 v[40:41], v[28:29], v[40:41]
	v_med3_f32 v42, v38, s53, v115
	v_med3_f32 v43, v39, s53, v115
	v_cvt_pk_fp8_f32 v44, v42, v43
	v_pk_mul_f32 v[34:35], v[34:35], v[78:79] op_sel_hi:[1,0]
	v_med3_f32 v42, v40, s53, v115
	v_med3_f32 v43, v41, s53, v115
	v_pk_mul_f32 v[34:35], v[30:31], v[34:35]
	v_cvt_pk_fp8_f32 v44, v42, v43 op_sel:[0,0,1]
	v_med3_f32 v42, v34, s53, v115
	v_med3_f32 v43, v35, s53, v115
	v_cvt_pk_fp8_f32 v45, v42, v43
	v_pk_mul_f32 v[36:37], v[36:37], v[78:79] op_sel_hi:[1,0]
	v_addc_co_u32_e32 v93, vcc, 0, v89, vcc
	v_pk_mul_f32 v[36:37], v[32:33], v[36:37]
	s_nop 0
	v_med3_f32 v42, v36, s53, v115
	v_med3_f32 v43, v37, s53, v115
	v_cvt_pk_fp8_f32 v45, v42, v43 op_sel:[0,0,1]
	global_store_dword v[76:77], v79, off offset:1024
	global_store_dword v[76:77], v80, off offset:1280
	global_store_dword v[76:77], v44, off offset:1536
	global_store_dword v[76:77], v45, off offset:1792
	s_waitcnt vmcnt(8)
	v_mov_b64_e32 v[42:43], v[164:165]
	v_mov_b64_e32 v[44:45], v[166:167]
	v_mov_b64_e32 v[76:77], v[168:169]
	v_mov_b64_e32 v[78:79], v[170:171]
	v_mov_b64_e32 v[80:81], v[172:173]
	v_mov_b64_e32 v[82:83], v[174:175]
	v_mov_b64_e32 v[84:85], v[180:181]
	v_mov_b64_e32 v[86:87], v[182:183]
	v_mov_b64_e32 v[88:89], v[176:177]
	v_mov_b64_e32 v[90:91], v[178:179]
	v_mov_b64_e32 v[124:125], v[184:185]
	v_mov_b64_e32 v[126:127], v[186:187]
	v_mov_b64_e32 v[128:129], v[192:193]
	v_mov_b64_e32 v[130:131], v[194:195]
	v_mov_b64_e32 v[132:133], v[188:189]
	v_mov_b64_e32 v[134:135], v[190:191]
	s_nop 0
	s_nop 0
	s_nop 0
	v_mov_b32_e32 v94, v43
	v_mov_b32_e32 v95, v77
	v_mov_b32_e32 v98, v45
	v_mov_b32_e32 v99, v79
	v_mov_b32_e32 v92, v42
	v_mov_b32_e32 v93, v76
	v_mov_b32_e32 v96, v44
	v_mov_b32_e32 v97, v78
	v_pk_mul_f32 v[94:95], v[94:95], v[94:95]
	v_pk_mul_f32 v[98:99], v[98:99], v[98:99]
	v_pk_fma_f32 v[92:93], v[92:93], v[92:93], v[94:95]
	v_pk_fma_f32 v[94:95], v[96:97], v[96:97], v[98:99]
	v_pk_mul_f32 v[96:97], v[80:81], v[80:81]
	v_pk_add_f32 v[92:93], v[92:93], v[94:95]
	v_pk_mul_f32 v[94:95], v[82:83], v[82:83]
	v_pk_add_f32 v[92:93], v[92:93], v[92:93] op_sel:[0,1] op_sel_hi:[1,0]
	v_pk_mov_b32 v[98:99], v[96:97], v[94:95] op_sel:[1,0]
	v_mov_b32_e32 v97, v95
	v_pk_add_f32 v[94:95], v[98:99], v[96:97]
	v_mul_f32_e32 v96, v84, v84
	v_mul_f32_e32 v97, v85, v85
	v_pk_add_f32 v[94:95], v[94:95], v[94:95] op_sel:[0,1] op_sel_hi:[1,0]
	v_mov_b32_e32 v93, v96
	v_mov_b32_e32 v95, v97
	v_pk_add_f32 v[92:93], v[92:93], v[94:95]
	v_mul_f32_e32 v94, v89, v89
	v_mul_f32_e32 v96, v91, v91
	v_mul_f32_e32 v98, v86, v86
	v_mul_f32_e32 v99, v87, v87
	v_pk_fma_f32 v[94:95], v[88:89], v[88:89], v[94:95] op_sel_hi:[1,1,0]
	v_pk_fma_f32 v[96:97], v[90:91], v[90:91], v[96:97] op_sel_hi:[1,1,0]
	v_mov_b32_e32 v95, v98
	v_mov_b32_e32 v97, v99
	v_pk_add_f32 v[94:95], v[94:95], v[96:97]
	v_pk_mul_f32 v[96:97], v[124:125], v[124:125]
	v_pk_add_f32 v[92:93], v[92:93], v[94:95]
	v_pk_mul_f32 v[94:95], v[126:127], v[126:127]
	v_pk_add_f32 v[92:93], v[92:93], v[92:93] op_sel:[0,1] op_sel_hi:[1,0]
	v_pk_mov_b32 v[98:99], v[96:97], v[94:95] op_sel:[1,0]
	v_mov_b32_e32 v97, v95
	v_pk_add_f32 v[94:95], v[98:99], v[96:97]
	v_mul_f32_e32 v96, v128, v128
	v_mul_f32_e32 v97, v129, v129
	v_pk_add_f32 v[94:95], v[94:95], v[94:95] op_sel:[0,1] op_sel_hi:[1,0]
	v_mov_b32_e32 v93, v96
	v_mov_b32_e32 v95, v97
	v_pk_add_f32 v[92:93], v[92:93], v[94:95]
	v_mul_f32_e32 v94, v133, v133
	v_mul_f32_e32 v96, v135, v135
	v_mul_f32_e32 v98, v130, v130
	v_mul_f32_e32 v99, v131, v131
	v_pk_fma_f32 v[94:95], v[132:133], v[132:133], v[94:95] op_sel_hi:[1,1,0]
	v_pk_fma_f32 v[96:97], v[134:135], v[134:135], v[96:97] op_sel_hi:[1,1,0]
	v_mov_b32_e32 v95, v98
	v_mov_b32_e32 v97, v99
	v_pk_add_f32 v[94:95], v[94:95], v[96:97]
	s_nop 0
	v_pk_add_f32 v[92:93], v[92:93], v[94:95]
	s_nop 0
	v_add_f32_e32 v92, v92, v93
	ds_bpermute_b32 v93, v118, v92
	s_waitcnt lgkmcnt(0)
	v_add_f32_e32 v92, v92, v93
	ds_bpermute_b32 v93, v119, v92
	s_waitcnt lgkmcnt(0)
	v_add_f32_e32 v92, v92, v93
	ds_bpermute_b32 v93, v120, v92
	s_waitcnt lgkmcnt(0)
	v_add_f32_e32 v92, v92, v93
	ds_bpermute_b32 v93, v121, v92
	s_waitcnt lgkmcnt(0)
	v_add_f32_e32 v92, v92, v93
	ds_bpermute_b32 v93, v122, v92
	s_waitcnt lgkmcnt(0)
	v_add_f32_e32 v92, v92, v93
	ds_bpermute_b32 v93, v123, v92
	s_waitcnt lgkmcnt(0)
	v_add_f32_e32 v92, v92, v93
	v_fmamk_f32 v92, v92, 0x3a000000, v114
	v_mul_f32_e32 v93, 0x4b800000, v92
	v_cmp_gt_f32_e32 vcc, s52, v92
	s_nop 1
	v_cndmask_b32_e32 v92, v92, v93, vcc
	v_rsq_f32_e32 v92, v92
	s_nop 0
	v_mul_f32_e32 v93, 0x45800000, v92
	v_cndmask_b32_e32 v136, v92, v93, vcc
	v_pk_mul_f32 v[44:45], v[44:45], v[136:137] op_sel_hi:[1,0]
	v_pk_mul_f32 v[42:43], v[42:43], v[136:137] op_sel_hi:[1,0]
	v_pk_mul_f32 v[104:105], v[4:5], v[44:45]
	v_pk_mul_f32 v[44:45], v[76:77], v[136:137] op_sel_hi:[1,0]
	v_pk_mul_f32 v[76:77], v[78:79], v[136:137] op_sel_hi:[1,0]
	v_pk_mul_f32 v[102:103], v[6:7], v[44:45]
	v_med3_f32 v44, v102, s53, v115
	v_med3_f32 v45, v103, s53, v115
	v_cvt_pk_fp8_f32 v78, v44, v45
	v_pk_mul_f32 v[100:101], v[2:3], v[42:43]
	v_pk_mul_f32 v[98:99], v[8:9], v[76:77]
	v_med3_f32 v42, v100, s53, v115
	v_med3_f32 v43, v101, s53, v115
	v_med3_f32 v44, v98, s53, v115
	v_med3_f32 v45, v99, s53, v115
	v_cvt_pk_fp8_f32 v92, v42, v43
	v_cvt_pk_fp8_f32 v78, v44, v45 op_sel:[0,0,1]
	v_pk_mul_f32 v[44:45], v[80:81], v[136:137] op_sel_hi:[1,0]
	v_pk_mul_f32 v[94:95], v[10:11], v[44:45]
	v_med3_f32 v42, v104, s53, v115
	v_med3_f32 v44, v94, s53, v115
	v_med3_f32 v45, v95, s53, v115
	v_med3_f32 v43, v105, s53, v115
	v_cvt_pk_fp8_f32 v79, v44, v45
	v_cvt_pk_fp8_f32 v92, v42, v43 op_sel:[0,0,1]
	v_pk_mul_f32 v[76:77], v[82:83], v[136:137] op_sel_hi:[1,0]
	v_lshl_add_u64 v[42:43], v[52:53], 0, s[12:13]
	v_pk_mul_f32 v[96:97], v[12:13], v[76:77]
	global_store_dword v[42:43], v92, off
	v_med3_f32 v44, v96, s53, v115
	v_med3_f32 v45, v97, s53, v115
	v_cvt_pk_fp8_f32 v79, v44, v45 op_sel:[0,0,1]
	v_pk_mul_f32 v[44:45], v[88:89], v[136:137] op_sel_hi:[1,0]
	v_pk_mul_f32 v[92:93], v[14:15], v[44:45]
	v_pk_mul_f32 v[76:77], v[90:91], v[136:137] op_sel_hi:[1,0]
	v_med3_f32 v44, v92, s53, v115
	v_med3_f32 v45, v93, s53, v115
	v_cvt_pk_fp8_f32 v80, v44, v45
	v_pk_mul_f32 v[90:91], v[16:17], v[76:77]
	v_med3_f32 v44, v90, s53, v115
	v_med3_f32 v45, v91, s53, v115
	v_cvt_pk_fp8_f32 v80, v44, v45 op_sel:[0,0,1]
	v_pk_mul_f32 v[44:45], v[84:85], v[136:137] op_sel_hi:[1,0]
	v_pk_mul_f32 v[76:77], v[86:87], v[136:137] op_sel_hi:[1,0]
	v_pk_mul_f32 v[82:83], v[18:19], v[44:45]
	v_pk_mul_f32 v[88:89], v[20:21], v[76:77]
	v_med3_f32 v44, v82, s53, v115
	v_med3_f32 v45, v83, s53, v115
	v_cvt_pk_fp8_f32 v81, v44, v45
	v_med3_f32 v44, v88, s53, v115
	v_med3_f32 v45, v89, s53, v115
	v_pk_mul_f32 v[76:77], v[126:127], v[136:137] op_sel_hi:[1,0]
	v_cvt_pk_fp8_f32 v81, v44, v45 op_sel:[0,0,1]
	v_pk_mul_f32 v[44:45], v[124:125], v[136:137] op_sel_hi:[1,0]
	v_pk_mul_f32 v[86:87], v[22:23], v[44:45]
	v_pk_mul_f32 v[84:85], v[24:25], v[76:77]
	v_med3_f32 v44, v86, s53, v115
	v_med3_f32 v45, v87, s53, v115
	v_cvt_pk_fp8_f32 v124, v44, v45
	v_med3_f32 v44, v84, s53, v115
	v_med3_f32 v45, v85, s53, v115
	global_store_dword v[42:43], v78, off offset:256
	global_store_dword v[42:43], v79, off offset:512
	global_store_dword v[42:43], v80, off offset:768
	global_store_dword v[42:43], v81, off offset:1024
	v_cvt_pk_fp8_f32 v124, v44, v45 op_sel:[0,0,1]
	v_pk_mul_f32 v[44:45], v[132:133], v[136:137] op_sel_hi:[1,0]
	v_pk_mul_f32 v[78:79], v[26:27], v[44:45]
	v_pk_mul_f32 v[76:77], v[134:135], v[136:137] op_sel_hi:[1,0]
	v_med3_f32 v44, v78, s53, v115
	v_med3_f32 v45, v79, s53, v115
	v_cvt_pk_fp8_f32 v125, v44, v45
	v_pk_mul_f32 v[80:81], v[28:29], v[76:77]
	v_pk_mul_f32 v[76:77], v[128:129], v[136:137] op_sel_hi:[1,0]
	v_med3_f32 v44, v80, s53, v115
	v_med3_f32 v45, v81, s53, v115
	v_cvt_pk_fp8_f32 v125, v44, v45 op_sel:[0,0,1]
	v_pk_mul_f32 v[44:45], v[130:131], v[136:137] op_sel_hi:[1,0]
	ds_read_b128 v[128:131], v1
	v_pk_mul_f32 v[76:77], v[30:31], v[76:77]
	v_mov_b32_e32 v126, 0
	v_med3_f32 v127, v76, s53, v115
	v_med3_f32 v132, v77, s53, v115
	v_cvt_pk_fp8_f32 v126, v127, v132
	ds_read_b128 v[132:135], v1 offset:1024
	s_waitcnt lgkmcnt(1)
	v_mul_f32_e32 v127, v75, v129
	v_mul_f32_e32 v129, v101, v129
	v_fmac_f32_e32 v127, v74, v128
	v_fmac_f32_e32 v129, v100, v128
	v_mul_f32_e32 v128, v105, v131
	v_mul_f32_e32 v136, v73, v131
	v_fmac_f32_e32 v128, v104, v130
	v_fmac_f32_e32 v136, v72, v130
	v_add_f32_e32 v128, v129, v128
	v_add_f32_e32 v127, v127, v136
	v_add_f32_e32 v136, 0, v128
	s_waitcnt lgkmcnt(0)
	v_mul_f32_e32 v128, v71, v133
	v_mul_f32_e32 v129, v69, v135
	v_fmac_f32_e32 v128, v70, v132
	v_fmac_f32_e32 v129, v68, v134
	v_add_f32_e32 v127, 0, v127
	v_add_f32_e32 v128, v128, v129
	v_add_f32_e32 v127, v127, v128
	v_mul_f32_e32 v133, v103, v133
	ds_read_b128 v[128:131], v1 offset:2048
	v_fmac_f32_e32 v133, v102, v132
	v_mul_f32_e32 v132, v99, v135
	v_fmac_f32_e32 v132, v98, v134
	v_add_f32_e32 v132, v133, v132
	v_add_f32_e32 v136, v136, v132
	ds_read_b128 v[132:135], v1 offset:3072
	s_waitcnt lgkmcnt(1)
	v_mul_f32_e32 v137, v65, v129
	v_mul_f32_e32 v129, v95, v129
	v_fmac_f32_e32 v137, v64, v128
	v_fmac_f32_e32 v129, v94, v128
	v_mul_f32_e32 v128, v97, v131
	v_fmac_f32_e32 v128, v96, v130
	v_mul_f32_e32 v138, v61, v131
	v_add_f32_e32 v128, v129, v128
	v_fmac_f32_e32 v138, v60, v130
	v_add_f32_e32 v136, v136, v128
	s_waitcnt lgkmcnt(0)
	v_mul_f32_e32 v128, v57, v133
	v_mul_f32_e32 v129, v67, v135
	v_add_f32_e32 v137, v137, v138
	v_fmac_f32_e32 v128, v56, v132
	v_fmac_f32_e32 v129, v66, v134
	v_add_f32_e32 v127, v127, v137
	v_add_f32_e32 v128, v128, v129
	v_add_f32_e32 v127, v127, v128
	v_mul_f32_e32 v133, v93, v133
	ds_read_b128 v[128:131], v1 offset:4096
	v_fmac_f32_e32 v133, v92, v132
	v_mul_f32_e32 v132, v91, v135
	v_fmac_f32_e32 v132, v90, v134
	v_add_f32_e32 v132, v133, v132
	v_add_f32_e32 v136, v136, v132
	ds_read_b128 v[132:135], v1 offset:5120
	s_waitcnt lgkmcnt(1)
	v_mul_f32_e32 v137, v59, v129
	v_mul_f32_e32 v129, v83, v129
	v_fmac_f32_e32 v137, v58, v128
	v_fmac_f32_e32 v129, v82, v128
	v_mul_f32_e32 v128, v89, v131
	v_fmac_f32_e32 v128, v88, v130
	v_mul_f32_e32 v138, v63, v131
	v_add_f32_e32 v128, v129, v128
	v_fmac_f32_e32 v138, v62, v130
	v_add_f32_e32 v136, v136, v128
	s_waitcnt lgkmcnt(0)
	v_mul_f32_e32 v128, v47, v133
	v_mul_f32_e32 v129, v49, v135
	v_add_f32_e32 v137, v137, v138
	v_fmac_f32_e32 v128, v46, v132
	v_fmac_f32_e32 v129, v48, v134
	v_add_f32_e32 v127, v127, v137
	v_add_f32_e32 v128, v128, v129
	v_add_f32_e32 v127, v127, v128
	v_mul_f32_e32 v133, v87, v133
	ds_read_b128 v[128:131], v1 offset:6144
	v_fmac_f32_e32 v133, v86, v132
	v_mul_f32_e32 v132, v85, v135
	v_fmac_f32_e32 v132, v84, v134
	v_add_f32_e32 v132, v133, v132
	v_add_f32_e32 v136, v136, v132
	ds_read_b128 v[132:135], v1 offset:7168
	s_waitcnt lgkmcnt(1)
	v_mul_f32_e32 v137, v39, v129
	v_mul_f32_e32 v129, v79, v129
	v_fmac_f32_e32 v137, v38, v128
	v_fmac_f32_e32 v129, v78, v128
	v_mul_f32_e32 v128, v81, v131
	v_fmac_f32_e32 v128, v80, v130
	v_mul_f32_e32 v138, v41, v131
	v_add_f32_e32 v128, v129, v128
	v_fmac_f32_e32 v138, v40, v130
	v_add_f32_e32 v129, v136, v128
	s_waitcnt lgkmcnt(0)
	v_mul_f32_e32 v128, v35, v133
	v_mul_f32_e32 v130, v37, v135
	v_add_f32_e32 v137, v137, v138
	v_fmac_f32_e32 v128, v34, v132
	v_fmac_f32_e32 v130, v36, v134
	v_add_f32_e32 v127, v127, v137
	v_add_f32_e32 v128, v128, v130
	v_add_f32_e32 v128, v127, v128
	v_mul_f32_e32 v127, v77, v133
	v_fmac_f32_e32 v127, v76, v132
	ds_read_b128 v[130:133], v1 offset:8192
	v_pk_mul_f32 v[44:45], v[32:33], v[44:45]
	s_nop 0
	v_mul_f32_e32 v135, v45, v135
	v_fmac_f32_e32 v135, v44, v134
	v_add_f32_e32 v127, v127, v135
	ds_read_b128 v[134:137], v1 offset:9216
	v_add_f32_e32 v127, v129, v127
	s_waitcnt lgkmcnt(1)
	v_mul_f32_e32 v129, v75, v131
	v_mul_f32_e32 v131, v101, v131
	v_fmac_f32_e32 v129, v74, v130
	v_fmac_f32_e32 v131, v100, v130
	v_mul_f32_e32 v130, v105, v133
	v_mul_f32_e32 v138, v73, v133
	v_fmac_f32_e32 v130, v104, v132
	v_fmac_f32_e32 v138, v72, v132
	v_add_f32_e32 v130, v131, v130
	v_add_f32_e32 v129, v129, v138
	v_add_f32_e32 v138, 0, v130
	s_waitcnt lgkmcnt(0)
	v_mul_f32_e32 v130, v71, v135
	v_mul_f32_e32 v131, v69, v137
	v_fmac_f32_e32 v130, v70, v134
	v_fmac_f32_e32 v131, v68, v136
	v_add_f32_e32 v129, 0, v129
	v_add_f32_e32 v130, v130, v131
	v_add_f32_e32 v129, v129, v130
	v_mul_f32_e32 v135, v103, v135
	ds_read_b128 v[130:133], v1 offset:10240
	v_fmac_f32_e32 v135, v102, v134
	v_mul_f32_e32 v134, v99, v137
	v_fmac_f32_e32 v134, v98, v136
	v_add_f32_e32 v134, v135, v134
	v_add_f32_e32 v138, v138, v134
	ds_read_b128 v[134:137], v1 offset:11264
	s_waitcnt lgkmcnt(1)
	v_mul_f32_e32 v139, v65, v131
	v_mul_f32_e32 v131, v95, v131
	v_fmac_f32_e32 v139, v64, v130
	v_fmac_f32_e32 v131, v94, v130
	v_mul_f32_e32 v130, v97, v133
	v_fmac_f32_e32 v130, v96, v132
	v_mul_f32_e32 v140, v61, v133
	v_add_f32_e32 v130, v131, v130
	v_fmac_f32_e32 v140, v60, v132
	v_add_f32_e32 v138, v138, v130
	s_waitcnt lgkmcnt(0)
	v_mul_f32_e32 v130, v57, v135
	v_mul_f32_e32 v131, v67, v137
	v_add_f32_e32 v139, v139, v140
	v_fmac_f32_e32 v130, v56, v134
	v_fmac_f32_e32 v131, v66, v136
	v_add_f32_e32 v129, v129, v139
	v_add_f32_e32 v130, v130, v131
	v_add_f32_e32 v129, v129, v130
	v_mul_f32_e32 v135, v93, v135
	ds_read_b128 v[130:133], v1 offset:12288
	v_fmac_f32_e32 v135, v92, v134
	v_mul_f32_e32 v134, v91, v137
	v_fmac_f32_e32 v134, v90, v136
	v_add_f32_e32 v134, v135, v134
	v_add_f32_e32 v138, v138, v134
	ds_read_b128 v[134:137], v1 offset:13312
	s_waitcnt lgkmcnt(1)
	v_mul_f32_e32 v139, v59, v131
	v_mul_f32_e32 v131, v83, v131
	v_fmac_f32_e32 v139, v58, v130
	v_fmac_f32_e32 v131, v82, v130
	v_mul_f32_e32 v130, v89, v133
	v_fmac_f32_e32 v130, v88, v132
	v_mul_f32_e32 v140, v63, v133
	v_add_f32_e32 v130, v131, v130
	v_fmac_f32_e32 v140, v62, v132
	v_add_f32_e32 v138, v138, v130
	s_waitcnt lgkmcnt(0)
	v_mul_f32_e32 v130, v47, v135
	v_mul_f32_e32 v131, v49, v137
	v_add_f32_e32 v139, v139, v140
	v_fmac_f32_e32 v130, v46, v134
	v_fmac_f32_e32 v131, v48, v136
	v_add_f32_e32 v129, v129, v139
	v_add_f32_e32 v130, v130, v131
	v_add_f32_e32 v129, v129, v130
	v_mul_f32_e32 v135, v87, v135
	ds_read_b128 v[130:133], v1 offset:14336
	v_fmac_f32_e32 v135, v86, v134
	v_mul_f32_e32 v134, v85, v137
	v_fmac_f32_e32 v134, v84, v136
	v_add_f32_e32 v134, v135, v134
	v_add_f32_e32 v138, v138, v134
	ds_read_b128 v[134:137], v1 offset:15360
	s_waitcnt lgkmcnt(1)
	v_mul_f32_e32 v139, v39, v131
	v_mul_f32_e32 v131, v79, v131
	v_fmac_f32_e32 v139, v38, v130
	v_fmac_f32_e32 v131, v78, v130
	v_mul_f32_e32 v130, v81, v133
	v_fmac_f32_e32 v130, v80, v132
	v_mul_f32_e32 v140, v41, v133
	v_add_f32_e32 v130, v131, v130
	v_fmac_f32_e32 v140, v40, v132
	v_add_f32_e32 v131, v138, v130
	s_waitcnt lgkmcnt(0)
	v_mul_f32_e32 v130, v35, v135
	v_mul_f32_e32 v132, v37, v137
	v_add_f32_e32 v139, v139, v140
	v_fmac_f32_e32 v130, v34, v134
	v_fmac_f32_e32 v132, v36, v136
	v_add_f32_e32 v129, v129, v139
	v_add_f32_e32 v130, v130, v132
	v_add_f32_e32 v130, v129, v130
	v_mul_f32_e32 v129, v77, v135
	v_fmac_f32_e32 v129, v76, v134
	ds_read_b128 v[132:135], v1 offset:16384
	v_mul_f32_e32 v137, v45, v137
	v_fmac_f32_e32 v137, v44, v136
	v_add_f32_e32 v129, v129, v137
	ds_read_b128 v[136:139], v1 offset:17408
	v_add_f32_e32 v129, v131, v129
	s_waitcnt lgkmcnt(1)
	v_mul_f32_e32 v131, v75, v133
	v_mul_f32_e32 v133, v101, v133
	v_fmac_f32_e32 v131, v74, v132
	v_fmac_f32_e32 v133, v100, v132
	v_mul_f32_e32 v132, v105, v135
	v_mul_f32_e32 v140, v73, v135
	v_fmac_f32_e32 v132, v104, v134
	v_fmac_f32_e32 v140, v72, v134
	v_add_f32_e32 v132, v133, v132
	v_add_f32_e32 v131, v131, v140
	v_add_f32_e32 v140, 0, v132
	s_waitcnt lgkmcnt(0)
	v_mul_f32_e32 v132, v71, v137
	v_mul_f32_e32 v133, v69, v139
	v_fmac_f32_e32 v132, v70, v136
	v_fmac_f32_e32 v133, v68, v138
	v_add_f32_e32 v131, 0, v131
	v_add_f32_e32 v132, v132, v133
	v_add_f32_e32 v131, v131, v132
	v_mul_f32_e32 v137, v103, v137
	ds_read_b128 v[132:135], v1 offset:18432
	v_fmac_f32_e32 v137, v102, v136
	v_mul_f32_e32 v136, v99, v139
	v_fmac_f32_e32 v136, v98, v138
	v_add_f32_e32 v136, v137, v136
	v_add_f32_e32 v140, v140, v136
	ds_read_b128 v[136:139], v1 offset:19456
	s_waitcnt lgkmcnt(1)
	v_mul_f32_e32 v141, v65, v133
	v_mul_f32_e32 v133, v95, v133
	v_fmac_f32_e32 v141, v64, v132
	v_fmac_f32_e32 v133, v94, v132
	v_mul_f32_e32 v132, v97, v135
	v_fmac_f32_e32 v132, v96, v134
	v_mul_f32_e32 v142, v61, v135
	v_add_f32_e32 v132, v133, v132
	v_fmac_f32_e32 v142, v60, v134
	v_add_f32_e32 v140, v140, v132
	s_waitcnt lgkmcnt(0)
	v_mul_f32_e32 v132, v57, v137
	v_mul_f32_e32 v133, v67, v139
	v_add_f32_e32 v141, v141, v142
	v_fmac_f32_e32 v132, v56, v136
	v_fmac_f32_e32 v133, v66, v138
	v_add_f32_e32 v131, v131, v141
	v_add_f32_e32 v132, v132, v133
	v_add_f32_e32 v131, v131, v132
	v_mul_f32_e32 v137, v93, v137
	ds_read_b128 v[132:135], v1 offset:20480
	v_fmac_f32_e32 v137, v92, v136
	v_mul_f32_e32 v136, v91, v139
	v_fmac_f32_e32 v136, v90, v138
	v_add_f32_e32 v136, v137, v136
	v_add_f32_e32 v140, v140, v136
	ds_read_b128 v[136:139], v1 offset:21504
	s_waitcnt lgkmcnt(1)
	v_mul_f32_e32 v141, v59, v133
	v_mul_f32_e32 v133, v83, v133
	v_fmac_f32_e32 v141, v58, v132
	v_fmac_f32_e32 v133, v82, v132
	v_mul_f32_e32 v132, v89, v135
	v_fmac_f32_e32 v132, v88, v134
	v_mul_f32_e32 v142, v63, v135
	v_add_f32_e32 v132, v133, v132
	v_fmac_f32_e32 v142, v62, v134
	v_add_f32_e32 v140, v140, v132
	s_waitcnt lgkmcnt(0)
	v_mul_f32_e32 v132, v47, v137
	v_mul_f32_e32 v133, v49, v139
	v_add_f32_e32 v141, v141, v142
	v_fmac_f32_e32 v132, v46, v136
	v_fmac_f32_e32 v133, v48, v138
	v_add_f32_e32 v131, v131, v141
	v_add_f32_e32 v132, v132, v133
	v_add_f32_e32 v131, v131, v132
	v_mul_f32_e32 v137, v87, v137
	ds_read_b128 v[132:135], v1 offset:22528
	v_fmac_f32_e32 v137, v86, v136
	v_mul_f32_e32 v136, v85, v139
	v_fmac_f32_e32 v136, v84, v138
	v_add_f32_e32 v136, v137, v136
	v_add_f32_e32 v140, v140, v136
	ds_read_b128 v[136:139], v1 offset:23552
	s_waitcnt lgkmcnt(1)
	v_mul_f32_e32 v141, v39, v133
	v_mul_f32_e32 v133, v79, v133
	v_fmac_f32_e32 v141, v38, v132
	v_fmac_f32_e32 v133, v78, v132
	v_mul_f32_e32 v132, v81, v135
	v_fmac_f32_e32 v132, v80, v134
	v_mul_f32_e32 v142, v41, v135
	v_add_f32_e32 v132, v133, v132
	v_fmac_f32_e32 v142, v40, v134
	v_add_f32_e32 v133, v140, v132
	s_waitcnt lgkmcnt(0)
	v_mul_f32_e32 v132, v35, v137
	v_mul_f32_e32 v134, v37, v139
	v_add_f32_e32 v141, v141, v142
	v_fmac_f32_e32 v132, v34, v136
	v_fmac_f32_e32 v134, v36, v138
	v_add_f32_e32 v131, v131, v141
	v_add_f32_e32 v132, v132, v134
	v_add_f32_e32 v132, v131, v132
	v_mul_f32_e32 v131, v77, v137
	v_fmac_f32_e32 v131, v76, v136
	ds_read_b128 v[134:137], v1 offset:24576
	v_mul_f32_e32 v139, v45, v139
	v_fmac_f32_e32 v139, v44, v138
	v_add_f32_e32 v131, v131, v139
	ds_read_b128 v[138:141], v1 offset:25600
	v_add_f32_e32 v131, v133, v131
	s_waitcnt lgkmcnt(1)
	v_mul_f32_e32 v133, v75, v135
	v_mul_f32_e32 v135, v101, v135
	v_fmac_f32_e32 v133, v74, v134
	v_fmac_f32_e32 v135, v100, v134
	v_mul_f32_e32 v134, v105, v137
	v_mul_f32_e32 v142, v73, v137
	v_fmac_f32_e32 v134, v104, v136
	v_fmac_f32_e32 v142, v72, v136
	v_add_f32_e32 v134, v135, v134
	v_add_f32_e32 v133, v133, v142
	v_add_f32_e32 v142, 0, v134
	s_waitcnt lgkmcnt(0)
	v_mul_f32_e32 v134, v71, v139
	v_mul_f32_e32 v135, v69, v141
	v_fmac_f32_e32 v134, v70, v138
	v_fmac_f32_e32 v135, v68, v140
	v_add_f32_e32 v133, 0, v133
	v_add_f32_e32 v134, v134, v135
	v_add_f32_e32 v133, v133, v134
	v_mul_f32_e32 v139, v103, v139
	ds_read_b128 v[134:137], v1 offset:26624
	v_fmac_f32_e32 v139, v102, v138
	v_mul_f32_e32 v138, v99, v141
	v_fmac_f32_e32 v138, v98, v140
	v_add_f32_e32 v138, v139, v138
	v_add_f32_e32 v142, v142, v138
	ds_read_b128 v[138:141], v1 offset:27648
	s_waitcnt lgkmcnt(1)
	v_mul_f32_e32 v143, v65, v135
	v_mul_f32_e32 v135, v95, v135
	v_fmac_f32_e32 v143, v64, v134
	v_fmac_f32_e32 v135, v94, v134
	v_mul_f32_e32 v134, v97, v137
	v_fmac_f32_e32 v134, v96, v136
	v_mul_f32_e32 v144, v61, v137
	v_add_f32_e32 v134, v135, v134
	v_fmac_f32_e32 v144, v60, v136
	v_add_f32_e32 v142, v142, v134
	s_waitcnt lgkmcnt(0)
	v_mul_f32_e32 v134, v57, v139
	v_mul_f32_e32 v135, v67, v141
	v_add_f32_e32 v143, v143, v144
	v_fmac_f32_e32 v134, v56, v138
	v_fmac_f32_e32 v135, v66, v140
	v_add_f32_e32 v133, v133, v143
	v_add_f32_e32 v134, v134, v135
	v_add_f32_e32 v133, v133, v134
	v_mul_f32_e32 v139, v93, v139
	ds_read_b128 v[134:137], v1 offset:28672
	v_fmac_f32_e32 v139, v92, v138
	v_mul_f32_e32 v138, v91, v141
	v_fmac_f32_e32 v138, v90, v140
	v_add_f32_e32 v138, v139, v138
	v_add_f32_e32 v142, v142, v138
	ds_read_b128 v[138:141], v1 offset:29696
	s_waitcnt lgkmcnt(1)
	v_mul_f32_e32 v143, v59, v135
	v_mul_f32_e32 v135, v83, v135
	v_fmac_f32_e32 v143, v58, v134
	v_fmac_f32_e32 v135, v82, v134
	v_mul_f32_e32 v134, v89, v137
	v_fmac_f32_e32 v134, v88, v136
	v_mul_f32_e32 v144, v63, v137
	v_add_f32_e32 v134, v135, v134
	v_fmac_f32_e32 v144, v62, v136
	v_add_f32_e32 v142, v142, v134
	s_waitcnt lgkmcnt(0)
	v_mul_f32_e32 v134, v47, v139
	v_mul_f32_e32 v135, v49, v141
	v_add_f32_e32 v143, v143, v144
	v_fmac_f32_e32 v134, v46, v138
	v_fmac_f32_e32 v135, v48, v140
	v_add_f32_e32 v133, v133, v143
	v_add_f32_e32 v134, v134, v135
	v_add_f32_e32 v133, v133, v134
	v_mul_f32_e32 v139, v87, v139
	ds_read_b128 v[134:137], v1 offset:30720
	v_fmac_f32_e32 v139, v86, v138
	v_mul_f32_e32 v138, v85, v141
	v_fmac_f32_e32 v138, v84, v140
	v_add_f32_e32 v138, v139, v138
	v_add_f32_e32 v142, v142, v138
	ds_read_b128 v[138:141], v1 offset:31744
	s_waitcnt lgkmcnt(1)
	v_mul_f32_e32 v143, v39, v135
	v_mul_f32_e32 v135, v79, v135
	v_fmac_f32_e32 v143, v38, v134
	v_fmac_f32_e32 v135, v78, v134
	v_mul_f32_e32 v134, v81, v137
	v_fmac_f32_e32 v134, v80, v136
	v_mul_f32_e32 v144, v41, v137
	v_add_f32_e32 v134, v135, v134
	v_fmac_f32_e32 v144, v40, v136
	v_add_f32_e32 v135, v142, v134
	s_waitcnt lgkmcnt(0)
	v_mul_f32_e32 v134, v35, v139
	v_mul_f32_e32 v136, v37, v141
	v_add_f32_e32 v143, v143, v144
	v_fmac_f32_e32 v134, v34, v138
	v_fmac_f32_e32 v136, v36, v140
	v_add_f32_e32 v133, v133, v143
	v_add_f32_e32 v134, v134, v136
	v_add_f32_e32 v134, v133, v134
	v_mul_f32_e32 v133, v77, v139
	v_fmac_f32_e32 v133, v76, v138
	ds_read_b128 v[136:139], v1 offset:32768
	v_mul_f32_e32 v141, v45, v141
	v_fmac_f32_e32 v141, v44, v140
	v_add_f32_e32 v133, v133, v141
	ds_read_b128 v[140:143], v1 offset:33792
	v_add_f32_e32 v133, v135, v133
	s_waitcnt lgkmcnt(1)
	v_mul_f32_e32 v135, v75, v137
	v_mul_f32_e32 v137, v101, v137
	v_fmac_f32_e32 v135, v74, v136
	v_fmac_f32_e32 v137, v100, v136
	v_mul_f32_e32 v136, v105, v139
	v_mul_f32_e32 v144, v73, v139
	v_fmac_f32_e32 v136, v104, v138
	v_fmac_f32_e32 v144, v72, v138
	v_add_f32_e32 v136, v137, v136
	v_add_f32_e32 v135, v135, v144
	v_add_f32_e32 v144, 0, v136
	s_waitcnt lgkmcnt(0)
	v_mul_f32_e32 v136, v71, v141
	v_mul_f32_e32 v137, v69, v143
	v_fmac_f32_e32 v136, v70, v140
	v_fmac_f32_e32 v137, v68, v142
	v_add_f32_e32 v135, 0, v135
	v_add_f32_e32 v136, v136, v137
	v_add_f32_e32 v135, v135, v136
	v_mul_f32_e32 v141, v103, v141
	ds_read_b128 v[136:139], v1 offset:34816
	v_fmac_f32_e32 v141, v102, v140
	v_mul_f32_e32 v140, v99, v143
	v_fmac_f32_e32 v140, v98, v142
	v_add_f32_e32 v140, v141, v140
	v_add_f32_e32 v144, v144, v140
	ds_read_b128 v[140:143], v1 offset:35840
	s_waitcnt lgkmcnt(1)
	v_mul_f32_e32 v145, v65, v137
	v_mul_f32_e32 v137, v95, v137
	v_fmac_f32_e32 v145, v64, v136
	v_fmac_f32_e32 v137, v94, v136
	v_mul_f32_e32 v136, v97, v139
	v_fmac_f32_e32 v136, v96, v138
	v_mul_f32_e32 v146, v61, v139
	v_add_f32_e32 v136, v137, v136
	v_fmac_f32_e32 v146, v60, v138
	v_add_f32_e32 v144, v144, v136
	s_waitcnt lgkmcnt(0)
	v_mul_f32_e32 v136, v57, v141
	v_mul_f32_e32 v137, v67, v143
	v_add_f32_e32 v145, v145, v146
	v_fmac_f32_e32 v136, v56, v140
	v_fmac_f32_e32 v137, v66, v142
	v_add_f32_e32 v135, v135, v145
	v_add_f32_e32 v136, v136, v137
	v_add_f32_e32 v135, v135, v136
	v_mul_f32_e32 v141, v93, v141
	ds_read_b128 v[136:139], v1 offset:36864
	v_fmac_f32_e32 v141, v92, v140
	v_mul_f32_e32 v140, v91, v143
	v_fmac_f32_e32 v140, v90, v142
	v_add_f32_e32 v140, v141, v140
	v_add_f32_e32 v144, v144, v140
	ds_read_b128 v[140:143], v1 offset:37888
	s_waitcnt lgkmcnt(1)
	v_mul_f32_e32 v145, v59, v137
	v_mul_f32_e32 v137, v83, v137
	v_fmac_f32_e32 v145, v58, v136
	v_fmac_f32_e32 v137, v82, v136
	v_mul_f32_e32 v136, v89, v139
	v_fmac_f32_e32 v136, v88, v138
	v_mul_f32_e32 v146, v63, v139
	v_add_f32_e32 v136, v137, v136
	v_fmac_f32_e32 v146, v62, v138
	v_add_f32_e32 v144, v144, v136
	s_waitcnt lgkmcnt(0)
	v_mul_f32_e32 v136, v47, v141
	v_mul_f32_e32 v137, v49, v143
	v_add_f32_e32 v145, v145, v146
	v_fmac_f32_e32 v136, v46, v140
	v_fmac_f32_e32 v137, v48, v142
	v_add_f32_e32 v135, v135, v145
	v_add_f32_e32 v136, v136, v137
	v_add_f32_e32 v135, v135, v136
	v_mul_f32_e32 v141, v87, v141
	ds_read_b128 v[136:139], v1 offset:38912
	v_fmac_f32_e32 v141, v86, v140
	v_mul_f32_e32 v140, v85, v143
	v_fmac_f32_e32 v140, v84, v142
	v_add_f32_e32 v140, v141, v140
	v_add_f32_e32 v144, v144, v140
	ds_read_b128 v[140:143], v1 offset:39936
	s_waitcnt lgkmcnt(1)
	v_mul_f32_e32 v145, v39, v137
	v_mul_f32_e32 v137, v79, v137
	v_fmac_f32_e32 v145, v38, v136
	v_fmac_f32_e32 v137, v78, v136
	v_mul_f32_e32 v136, v81, v139
	v_fmac_f32_e32 v136, v80, v138
	v_mul_f32_e32 v146, v41, v139
	v_add_f32_e32 v136, v137, v136
	v_fmac_f32_e32 v146, v40, v138
	v_add_f32_e32 v137, v144, v136
	s_waitcnt lgkmcnt(0)
	v_mul_f32_e32 v136, v35, v141
	v_mul_f32_e32 v138, v37, v143
	v_add_f32_e32 v145, v145, v146
	v_fmac_f32_e32 v136, v34, v140
	v_fmac_f32_e32 v138, v36, v142
	v_add_f32_e32 v135, v135, v145
	v_add_f32_e32 v136, v136, v138
	v_add_f32_e32 v136, v135, v136
	v_mul_f32_e32 v135, v77, v141
	v_fmac_f32_e32 v135, v76, v140
	ds_read_b128 v[138:141], v1 offset:40960
	v_mul_f32_e32 v143, v45, v143
	v_fmac_f32_e32 v143, v44, v142
	v_add_f32_e32 v135, v135, v143
	ds_read_b128 v[142:145], v1 offset:41984
	v_add_f32_e32 v135, v137, v135
	s_waitcnt lgkmcnt(1)
	v_mul_f32_e32 v137, v75, v139
	v_mul_f32_e32 v139, v101, v139
	v_fmac_f32_e32 v137, v74, v138
	v_fmac_f32_e32 v139, v100, v138
	v_mul_f32_e32 v138, v105, v141
	v_mul_f32_e32 v146, v73, v141
	v_fmac_f32_e32 v138, v104, v140
	v_fmac_f32_e32 v146, v72, v140
	v_add_f32_e32 v138, v139, v138
	v_add_f32_e32 v137, v137, v146
	v_add_f32_e32 v146, 0, v138
	s_waitcnt lgkmcnt(0)
	v_mul_f32_e32 v138, v71, v143
	v_mul_f32_e32 v139, v69, v145
	v_fmac_f32_e32 v138, v70, v142
	v_fmac_f32_e32 v139, v68, v144
	v_add_f32_e32 v137, 0, v137
	v_add_f32_e32 v138, v138, v139
	v_add_f32_e32 v137, v137, v138
	v_mul_f32_e32 v143, v103, v143
	ds_read_b128 v[138:141], v1 offset:43008
	v_fmac_f32_e32 v143, v102, v142
	v_mul_f32_e32 v142, v99, v145
	v_fmac_f32_e32 v142, v98, v144
	v_add_f32_e32 v142, v143, v142
	v_add_f32_e32 v146, v146, v142
	ds_read_b128 v[142:145], v1 offset:44032
	s_waitcnt lgkmcnt(1)
	v_mul_f32_e32 v147, v65, v139
	v_mul_f32_e32 v139, v95, v139
	v_fmac_f32_e32 v147, v64, v138
	v_fmac_f32_e32 v139, v94, v138
	v_mul_f32_e32 v138, v97, v141
	v_fmac_f32_e32 v138, v96, v140
	v_mul_f32_e32 v148, v61, v141
	v_add_f32_e32 v138, v139, v138
	v_fmac_f32_e32 v148, v60, v140
	v_add_f32_e32 v146, v146, v138
	s_waitcnt lgkmcnt(0)
	v_mul_f32_e32 v138, v57, v143
	v_mul_f32_e32 v139, v67, v145
	v_add_f32_e32 v147, v147, v148
	v_fmac_f32_e32 v138, v56, v142
	v_fmac_f32_e32 v139, v66, v144
	v_add_f32_e32 v137, v137, v147
	v_add_f32_e32 v138, v138, v139
	v_add_f32_e32 v137, v137, v138
	v_mul_f32_e32 v143, v93, v143
	ds_read_b128 v[138:141], v1 offset:45056
	v_fmac_f32_e32 v143, v92, v142
	v_mul_f32_e32 v142, v91, v145
	v_fmac_f32_e32 v142, v90, v144
	v_add_f32_e32 v142, v143, v142
	v_add_f32_e32 v146, v146, v142
	ds_read_b128 v[142:145], v1 offset:46080
	s_waitcnt lgkmcnt(1)
	v_mul_f32_e32 v147, v59, v139
	v_mul_f32_e32 v139, v83, v139
	v_fmac_f32_e32 v147, v58, v138
	v_fmac_f32_e32 v139, v82, v138
	v_mul_f32_e32 v138, v89, v141
	v_fmac_f32_e32 v138, v88, v140
	v_mul_f32_e32 v148, v63, v141
	v_add_f32_e32 v138, v139, v138
	v_fmac_f32_e32 v148, v62, v140
	v_add_f32_e32 v146, v146, v138
	s_waitcnt lgkmcnt(0)
	v_mul_f32_e32 v138, v47, v143
	v_mul_f32_e32 v139, v49, v145
	v_add_f32_e32 v147, v147, v148
	v_fmac_f32_e32 v138, v46, v142
	v_fmac_f32_e32 v139, v48, v144
	v_add_f32_e32 v137, v137, v147
	v_add_f32_e32 v138, v138, v139
	v_add_f32_e32 v137, v137, v138
	v_mul_f32_e32 v143, v87, v143
	ds_read_b128 v[138:141], v1 offset:47104
	v_fmac_f32_e32 v143, v86, v142
	v_mul_f32_e32 v142, v85, v145
	v_fmac_f32_e32 v142, v84, v144
	v_add_f32_e32 v142, v143, v142
	v_add_f32_e32 v146, v146, v142
	ds_read_b128 v[142:145], v1 offset:48128
	s_waitcnt lgkmcnt(1)
	v_mul_f32_e32 v147, v39, v139
	v_mul_f32_e32 v139, v79, v139
	v_fmac_f32_e32 v147, v38, v138
	v_fmac_f32_e32 v139, v78, v138
	v_mul_f32_e32 v138, v81, v141
	v_fmac_f32_e32 v138, v80, v140
	v_mul_f32_e32 v148, v41, v141
	v_add_f32_e32 v138, v139, v138
	v_fmac_f32_e32 v148, v40, v140
	v_add_f32_e32 v146, v146, v138
	s_waitcnt lgkmcnt(0)
	v_mul_f32_e32 v138, v35, v143
	v_mul_f32_e32 v139, v37, v145
	v_add_f32_e32 v147, v147, v148
	v_fmac_f32_e32 v138, v34, v142
	v_fmac_f32_e32 v139, v36, v144
	v_add_f32_e32 v137, v137, v147
	v_add_f32_e32 v138, v138, v139
	v_add_f32_e32 v137, v137, v138
	v_mul_f32_e32 v143, v77, v143
	ds_read_b128 v[138:141], v1 offset:49152
	v_fmac_f32_e32 v143, v76, v142
	v_mul_f32_e32 v142, v45, v145
	v_fmac_f32_e32 v142, v44, v144
	v_add_f32_e32 v142, v143, v142
	v_add_f32_e32 v146, v146, v142
	ds_read_b128 v[142:145], v1 offset:50176
	s_waitcnt lgkmcnt(1)
	v_mul_f32_e32 v147, v75, v139
	v_mul_f32_e32 v139, v101, v139
	v_fmac_f32_e32 v147, v74, v138
	v_fmac_f32_e32 v139, v100, v138
	v_mul_f32_e32 v138, v105, v141
	v_mul_f32_e32 v148, v73, v141
	v_fmac_f32_e32 v138, v104, v140
	v_fmac_f32_e32 v148, v72, v140
	v_add_f32_e32 v138, v139, v138
	v_add_f32_e32 v147, v147, v148
	v_add_f32_e32 v148, 0, v138
	s_waitcnt lgkmcnt(0)
	v_mul_f32_e32 v138, v71, v143
	v_mul_f32_e32 v139, v69, v145
	v_fmac_f32_e32 v138, v70, v142
	v_fmac_f32_e32 v139, v68, v144
	v_add_f32_e32 v147, 0, v147
	v_add_f32_e32 v138, v138, v139
	v_add_f32_e32 v147, v147, v138
	v_mul_f32_e32 v143, v103, v143
	ds_read_b128 v[138:141], v1 offset:51200
	v_fmac_f32_e32 v143, v102, v142
	v_mul_f32_e32 v142, v99, v145
	v_fmac_f32_e32 v142, v98, v144
	v_add_f32_e32 v142, v143, v142
	v_add_f32_e32 v148, v148, v142
	ds_read_b128 v[142:145], v1 offset:52224
	s_waitcnt lgkmcnt(1)
	v_mul_f32_e32 v149, v65, v139
	v_mul_f32_e32 v139, v95, v139
	v_fmac_f32_e32 v149, v64, v138
	v_fmac_f32_e32 v139, v94, v138
	v_mul_f32_e32 v138, v97, v141
	v_fmac_f32_e32 v138, v96, v140
	v_mul_f32_e32 v150, v61, v141
	v_add_f32_e32 v138, v139, v138
	v_fmac_f32_e32 v150, v60, v140
	v_add_f32_e32 v148, v148, v138
	s_waitcnt lgkmcnt(0)
	v_mul_f32_e32 v138, v57, v143
	v_mul_f32_e32 v139, v67, v145
	v_add_f32_e32 v149, v149, v150
	v_fmac_f32_e32 v138, v56, v142
	v_fmac_f32_e32 v139, v66, v144
	v_add_f32_e32 v147, v147, v149
	v_add_f32_e32 v138, v138, v139
	v_add_f32_e32 v147, v147, v138
	v_mul_f32_e32 v143, v93, v143
	ds_read_b128 v[138:141], v1 offset:53248
	v_fmac_f32_e32 v143, v92, v142
	v_mul_f32_e32 v142, v91, v145
	v_fmac_f32_e32 v142, v90, v144
	v_add_f32_e32 v142, v143, v142
	v_add_f32_e32 v148, v148, v142
	ds_read_b128 v[142:145], v1 offset:54272
	s_waitcnt lgkmcnt(1)
	v_mul_f32_e32 v149, v59, v139
	v_mul_f32_e32 v139, v83, v139
	v_fmac_f32_e32 v149, v58, v138
	v_fmac_f32_e32 v139, v82, v138
	v_mul_f32_e32 v138, v89, v141
	v_fmac_f32_e32 v138, v88, v140
	v_mul_f32_e32 v150, v63, v141
	v_add_f32_e32 v138, v139, v138
	v_fmac_f32_e32 v150, v62, v140
	v_add_f32_e32 v148, v148, v138
	s_waitcnt lgkmcnt(0)
	v_mul_f32_e32 v138, v47, v143
	v_mul_f32_e32 v139, v49, v145
	v_add_f32_e32 v149, v149, v150
	v_fmac_f32_e32 v138, v46, v142
	v_fmac_f32_e32 v139, v48, v144
	v_add_f32_e32 v147, v147, v149
	v_add_f32_e32 v138, v138, v139
	v_add_f32_e32 v147, v147, v138
	v_mul_f32_e32 v143, v87, v143
	ds_read_b128 v[138:141], v1 offset:55296
	v_fmac_f32_e32 v143, v86, v142
	v_mul_f32_e32 v142, v85, v145
	v_fmac_f32_e32 v142, v84, v144
	v_add_f32_e32 v142, v143, v142
	v_add_f32_e32 v148, v148, v142
	ds_read_b128 v[142:145], v1 offset:56320
	s_waitcnt lgkmcnt(1)
	v_mul_f32_e32 v149, v39, v139
	v_mul_f32_e32 v139, v79, v139
	v_fmac_f32_e32 v149, v38, v138
	v_fmac_f32_e32 v139, v78, v138
	v_mul_f32_e32 v138, v81, v141
	v_fmac_f32_e32 v138, v80, v140
	v_mul_f32_e32 v150, v41, v141
	v_add_f32_e32 v138, v139, v138
	v_fmac_f32_e32 v150, v40, v140
	v_add_f32_e32 v148, v148, v138
	s_waitcnt lgkmcnt(0)
	v_mul_f32_e32 v138, v35, v143
	v_mul_f32_e32 v139, v37, v145
	v_mul_f32_e32 v143, v77, v143
	v_add_f32_e32 v149, v149, v150
	v_fmac_f32_e32 v138, v34, v142
	v_fmac_f32_e32 v139, v36, v144
	v_fmac_f32_e32 v143, v76, v142
	v_mul_f32_e32 v142, v45, v145
	v_add_f32_e32 v147, v147, v149
	v_add_f32_e32 v138, v138, v139
	v_fmac_f32_e32 v142, v44, v144
	v_add_f32_e32 v147, v147, v138
	ds_read_b128 v[138:141], v1 offset:57344
	v_add_f32_e32 v142, v143, v142
	v_add_f32_e32 v148, v148, v142
	ds_read_b128 v[142:145], v1 offset:58368
	s_waitcnt lgkmcnt(1)
	v_mul_f32_e32 v75, v75, v139
	v_mul_f32_e32 v73, v73, v141
	v_fmac_f32_e32 v75, v74, v138
	v_fmac_f32_e32 v73, v72, v140
	s_waitcnt lgkmcnt(0)
	v_mul_f32_e32 v71, v71, v143
	v_mul_f32_e32 v69, v69, v145
	v_add_f32_e32 v72, v75, v73
	v_mul_f32_e32 v73, v101, v139
	v_mul_f32_e32 v74, v105, v141
	v_fmac_f32_e32 v71, v70, v142
	v_fmac_f32_e32 v69, v68, v144
	v_add_f32_e32 v72, 0, v72
	v_fmac_f32_e32 v73, v100, v138
	v_fmac_f32_e32 v74, v104, v140
	v_add_f32_e32 v68, v71, v69
	v_add_f32_e32 v73, v73, v74
	v_add_f32_e32 v100, v72, v68
	v_mul_f32_e32 v72, v103, v143
	v_mul_f32_e32 v74, v99, v145
	v_fmac_f32_e32 v72, v102, v142
	ds_read_b128 v[68:71], v1 offset:59392
	v_fmac_f32_e32 v74, v98, v144
	v_add_f32_e32 v73, 0, v73
	v_add_f32_e32 v72, v72, v74
	v_add_f32_e32 v98, v73, v72
	ds_read_b128 v[72:75], v1 offset:60416
	s_waitcnt lgkmcnt(1)
	v_mul_f32_e32 v65, v65, v69
	v_mul_f32_e32 v61, v61, v71
	v_fmac_f32_e32 v65, v64, v68
	v_fmac_f32_e32 v61, v60, v70
	v_add_f32_e32 v60, v65, v61
	v_mul_f32_e32 v61, v95, v69
	v_mul_f32_e32 v64, v97, v71
	s_waitcnt lgkmcnt(0)
	v_mul_f32_e32 v57, v57, v73
	v_fmac_f32_e32 v61, v94, v68
	v_fmac_f32_e32 v64, v96, v70
	v_fmac_f32_e32 v57, v56, v72
	v_mul_f32_e32 v56, v67, v75
	v_add_f32_e32 v61, v61, v64
	v_fmac_f32_e32 v56, v66, v74
	ds_read_b128 v[64:67], v1 offset:61440
	ds_read_b128 v[68:71], v1 offset:62464
	v_add_f32_e32 v60, v100, v60
	v_add_f32_e32 v56, v57, v56
	v_add_f32_e32 v56, v60, v56
	s_waitcnt lgkmcnt(1)
	v_mul_f32_e32 v59, v59, v65
	v_fmac_f32_e32 v59, v58, v64
	v_mul_f32_e32 v58, v63, v67
	v_fmac_f32_e32 v58, v62, v66
	v_mul_f32_e32 v57, v93, v73
	v_mul_f32_e32 v60, v91, v75
	v_add_f32_e32 v58, v59, v58
	s_waitcnt lgkmcnt(0)
	v_mul_f32_e32 v47, v47, v69
	v_fmac_f32_e32 v57, v92, v72
	v_fmac_f32_e32 v60, v90, v74
	v_add_f32_e32 v56, v56, v58
	v_mul_f32_e32 v58, v83, v65
	v_mul_f32_e32 v59, v89, v67
	v_fmac_f32_e32 v47, v46, v68
	v_mul_f32_e32 v46, v49, v71
	v_add_f32_e32 v61, v98, v61
	v_add_f32_e32 v57, v57, v60
	v_fmac_f32_e32 v58, v82, v64
	v_fmac_f32_e32 v59, v88, v66
	v_fmac_f32_e32 v46, v48, v70
	v_add_f32_e32 v57, v61, v57
	v_add_f32_e32 v58, v58, v59
	v_add_f32_e32 v46, v47, v46
	v_add_f32_e32 v57, v57, v58
	v_add_f32_e32 v60, v56, v46
	v_mul_f32_e32 v56, v87, v69
	v_mul_f32_e32 v58, v85, v71
	v_fmac_f32_e32 v56, v86, v68
	v_fmac_f32_e32 v58, v84, v70
	v_add_f32_e32 v56, v56, v58
	ds_read_b128 v[46:49], v1 offset:63488
	v_add_f32_e32 v61, v57, v56
	ds_read_b128 v[56:59], v1 offset:64512
	s_waitcnt lgkmcnt(1)
	v_mul_f32_e32 v39, v39, v47
	v_fmac_f32_e32 v39, v38, v46
	s_waitcnt lgkmcnt(0)
	v_mul_f32_e32 v35, v35, v57
	v_fmac_f32_e32 v35, v34, v56
	v_mul_f32_e32 v34, v37, v59
	v_fmac_f32_e32 v34, v36, v58
	v_cndmask_b32_e64 v36, v128, v136, s[0:1]
	v_mul_f32_e32 v38, v41, v49
	ds_bpermute_b32 v36, v123, v36
	v_fmac_f32_e32 v38, v40, v48
	v_add_f32_e32 v38, v39, v38
	v_add_f32_e32 v38, v60, v38
	v_add_f32_e32 v34, v35, v34
	v_add_f32_e32 v34, v38, v34
	v_cndmask_b32_e64 v38, v136, v128, s[0:1]
	v_mul_f32_e32 v39, v79, v47
	s_waitcnt lgkmcnt(0)
	v_add_f32_e32 v36, v38, v36
	v_cndmask_b32_e64 v38, v130, v137, s[0:1]
	v_fmac_f32_e32 v39, v78, v46
	ds_bpermute_b32 v38, v123, v38
	v_cndmask_b32_e64 v41, v132, v147, s[0:1]
	v_cndmask_b32_e64 v46, v134, v34, s[0:1]
	ds_bpermute_b32 v41, v123, v41
	ds_bpermute_b32 v46, v123, v46
	v_mul_f32_e32 v40, v81, v49
	v_fmac_f32_e32 v40, v80, v48
	v_add_f32_e32 v39, v39, v40
	v_cndmask_b32_e64 v40, v137, v130, s[0:1]
	s_waitcnt lgkmcnt(2)
	v_add_f32_e32 v38, v40, v38
	v_cndmask_b32_e64 v40, v147, v132, s[0:1]
	v_cndmask_b32_e64 v34, v34, v134, s[0:1]
	s_waitcnt lgkmcnt(1)
	v_add_f32_e32 v40, v40, v41
	s_waitcnt lgkmcnt(0)
	v_add_f32_e32 v34, v34, v46
	v_cndmask_b32_e64 v41, v36, v40, s[4:5]
	v_cndmask_b32_e64 v46, v38, v34, s[4:5]
	ds_bpermute_b32 v41, v122, v41
	ds_bpermute_b32 v46, v122, v46
	v_mul_f32_e32 v35, v77, v57
	v_mul_f32_e32 v37, v45, v59
	v_cndmask_b32_e64 v36, v40, v36, s[4:5]
	v_cndmask_b32_e64 v34, v34, v38, s[4:5]
	v_fmac_f32_e32 v35, v76, v56
	v_fmac_f32_e32 v37, v44, v58
	s_waitcnt lgkmcnt(1)
	v_add_f32_e32 v36, v36, v41
	s_waitcnt lgkmcnt(0)
	v_add_f32_e32 v34, v34, v46
	v_add_f32_e32 v35, v35, v37
	v_cndmask_b32_e64 v37, v36, v34, s[10:11]
	ds_bpermute_b32 v37, v121, v37
	v_add_f32_e32 v39, v61, v39
	v_cndmask_b32_e64 v38, v127, v135, s[0:1]
	v_cndmask_b32_e64 v34, v34, v36, s[10:11]
	ds_bpermute_b32 v38, v123, v38
	v_add_f32_e32 v35, v39, v35
	s_waitcnt lgkmcnt(1)
	v_add_f32_e32 v34, v34, v37
	v_cndmask_b32_e64 v37, v129, v146, s[0:1]
	ds_bpermute_b32 v37, v123, v37
	v_cndmask_b32_e64 v39, v131, v148, s[0:1]
	v_cndmask_b32_e64 v40, v133, v35, s[0:1]
	ds_bpermute_b32 v39, v123, v39
	ds_bpermute_b32 v40, v123, v40
	v_cndmask_b32_e64 v36, v135, v127, s[0:1]
	s_waitcnt lgkmcnt(3)
	v_add_f32_e32 v36, v36, v38
	v_cndmask_b32_e64 v38, v146, v129, s[0:1]
	s_waitcnt lgkmcnt(2)
	v_add_f32_e32 v37, v38, v37
	v_cndmask_b32_e64 v38, v148, v131, s[0:1]
	v_cndmask_b32_e64 v35, v35, v133, s[0:1]
	s_waitcnt lgkmcnt(1)
	v_add_f32_e32 v38, v38, v39
	s_waitcnt lgkmcnt(0)
	v_add_f32_e32 v35, v35, v40
	v_cndmask_b32_e64 v39, v36, v38, s[4:5]
	v_cndmask_b32_e64 v40, v37, v35, s[4:5]
	ds_bpermute_b32 v39, v122, v39
	ds_bpermute_b32 v40, v122, v40
	v_cndmask_b32_e64 v36, v38, v36, s[4:5]
	v_cndmask_b32_e64 v35, v35, v37, s[4:5]
	ds_bpermute_b32 v41, v120, v34
	s_waitcnt lgkmcnt(2)
	v_add_f32_e32 v36, v36, v39
	s_waitcnt lgkmcnt(1)
	v_add_f32_e32 v35, v35, v40
	v_cndmask_b32_e64 v37, v36, v35, s[10:11]
	ds_bpermute_b32 v37, v121, v37
	v_cndmask_b32_e64 v35, v35, v36, s[10:11]
	s_waitcnt lgkmcnt(1)
	v_add_f32_e32 v34, v34, v41
	ds_bpermute_b32 v39, v119, v34
	v_med3_f32 v38, v44, s53, v115
	s_waitcnt lgkmcnt(1)
	v_add_f32_e32 v35, v35, v37
	ds_bpermute_b32 v36, v120, v35
	v_med3_f32 v37, v45, s53, v115
	s_waitcnt lgkmcnt(1)
	v_add_f32_e32 v34, v34, v39
	v_cvt_pk_fp8_f32 v126, v38, v37 op_sel:[0,0,1]
	ds_bpermute_b32 v37, v118, v34
	s_waitcnt lgkmcnt(1)
	v_add_f32_e32 v35, v35, v36
	ds_bpermute_b32 v36, v119, v35
	global_store_dword v[42:43], v124, off offset:1280
	global_store_dword v[42:43], v125, off offset:1536
	global_store_dword v[42:43], v126, off offset:1792
	s_waitcnt lgkmcnt(1)
	v_add_f32_e32 v37, v34, v37
	s_nop 0
	v_readlane_b32 s60, v37, 0
	s_waitcnt lgkmcnt(0)
	v_add_f32_e32 v34, v35, v36
	ds_bpermute_b32 v35, v118, v34
	v_readlane_b32 s59, v37, 8
	v_readlane_b32 s41, v37, 16
	v_readlane_b32 s27, v37, 24
	v_readlane_b32 s26, v37, 32
	v_readlane_b32 s25, v37, 40
	v_readlane_b32 s24, v37, 48
	v_readlane_b32 s2, v37, 56
	s_and_saveexec_b64 s[42:43], s[6:7]
	s_cbranch_execz .LBB0_1349
	v_mov_b32_e32 v36, s60
	v_mov_b32_e32 v37, s59
	v_cmp_gt_f32_e32 vcc, s59, v36
	v_mov_b32_e32 v39, s41
	v_mov_b32_e32 v40, s27
	v_cndmask_b32_e32 v38, v36, v37, vcc
	v_cmp_gt_f32_e64 s[12:13], s41, v38
	v_mov_b32_e32 v41, s26
	v_mov_b32_e32 v42, s25
	v_cndmask_b32_e64 v38, v38, v39, s[12:13]
	v_cmp_gt_f32_e64 s[14:15], s27, v38
	v_mov_b32_e32 v43, s24
	v_cndmask_b32_e64 v45, 0, 1, vcc
	v_cndmask_b32_e64 v38, v38, v40, s[14:15]
	v_cmp_gt_f32_e64 s[16:17], s26, v38
	v_cmp_ngt_f32_e32 vcc, s60, v116
	v_mov_b32_e32 v44, s2
	v_cndmask_b32_e64 v38, v38, v41, s[16:17]
	v_cmp_gt_f32_e64 s[18:19], s25, v38
	s_mov_b64 s[44:45], exec
	s_nop 0
	v_cndmask_b32_e64 v38, v38, v42, s[18:19]
	v_cmp_gt_f32_e64 s[20:21], s24, v38
	s_nop 1
	v_cndmask_b32_e64 v38, v38, v43, s[20:21]
	v_cmp_ngt_f32_e64 s[22:23], s2, v38
	s_and_b64 s[62:63], s[20:21], s[22:23]
	s_and_b64 s[12:13], s[12:13], exec
	v_readfirstlane_b32 s12, v45
	s_cselect_b32 s61, 2, s12
	s_and_b64 s[12:13], s[14:15], exec
	s_cselect_b32 s14, 3, s61
	s_and_b64 s[12:13], s[16:17], exec
	s_cselect_b32 s14, 4, s14
	s_and_b64 s[12:13], s[18:19], exec
	s_cselect_b32 s14, 5, s14
	s_and_b64 s[12:13], s[20:21], exec
	s_cselect_b32 s14, 6, s14
	s_and_b64 s[12:13], s[22:23], exec
	s_cselect_b32 s61, s14, 7
	s_cmp_lg_u32 s61, 5
	s_cselect_b64 s[64:65], -1, 0
	s_cmp_lg_u32 s61, 4
	s_cselect_b64 s[20:21], -1, 0
	s_cmp_lg_u32 s61, 3
	s_cselect_b64 s[18:19], -1, 0
	s_cmp_lg_u32 s61, 2
	s_cselect_b64 s[16:17], -1, 0
	s_cmp_lg_u32 s61, 1
	s_cselect_b64 s[14:15], -1, 0
	s_cmp_eq_u32 s61, 0
	s_cselect_b64 s[12:13], -1, 0
	s_or_b64 vcc, s[12:13], vcc
	v_cndmask_b32_e32 v36, v36, v116, vcc
	v_cmp_gt_f32_e64 s[12:13], s59, v36
	s_and_b64 s[12:13], s[14:15], s[12:13]
	v_cndmask_b32_e64 v38, v44, v38, s[22:23]
	v_cndmask_b32_e64 v36, v36, v37, s[12:13]
	v_cmp_gt_f32_e64 s[14:15], s41, v36
	s_and_b64 s[14:15], s[16:17], s[14:15]
	v_cndmask_b32_e64 v37, 0, -1, vcc
	v_cndmask_b32_e64 v36, v36, v39, s[14:15]
	v_cmp_gt_f32_e64 s[16:17], s27, v36
	s_and_b64 s[16:17], s[18:19], s[16:17]
	s_nop 0
	v_cndmask_b32_e64 v36, v36, v40, s[16:17]
	v_cmp_gt_f32_e64 s[18:19], s26, v36
	s_and_b64 s[18:19], s[20:21], s[18:19]
	s_nop 0
	v_cndmask_b32_e64 v36, v36, v41, s[18:19]
	v_cmp_gt_f32_e64 s[20:21], s25, v36
	s_and_b64 s[20:21], s[64:65], s[20:21]
	s_nop 0
	v_cndmask_b32_e64 v36, v36, v42, s[20:21]
	v_cmp_ngt_f32_e64 s[24:25], s24, v36
	s_or_b64 s[24:25], s[62:63], s[24:25]
	s_nop 0
	v_cndmask_b32_e64 v36, v43, v36, s[24:25]
	v_cmp_gt_f32_e64 s[26:27], s2, v36
	s_and_b64 s[22:23], s[22:23], s[26:27]
	v_cndmask_b32_e64 v36, v36, v44, s[22:23]
	v_sub_f32_e32 v36, v36, v38
	v_readfirstlane_b32 s2, v37
	v_mul_f32_e32 v37, 0x3fb8aa3b, v36
	v_fma_f32 v38, v36, s54, -v37
	v_rndne_f32_e32 v39, v37
	v_fmac_f32_e32 v38, 0x32a5705f, v36
	v_sub_f32_e32 v37, v37, v39
	v_add_f32_e32 v37, v37, v38
	v_exp_f32_e32 v37, v37
	v_cvt_i32_f32_e32 v38, v39
	v_cmp_ngt_f32_e32 vcc, s55, v36
	s_and_b64 s[12:13], s[12:13], exec
	s_cselect_b32 s2, 1, s2
	v_ldexp_f32 v37, v37, v38
	v_cndmask_b32_e32 v37, 0, v37, vcc
	v_cmp_nlt_f32_e32 vcc, s56, v36
	s_and_b64 s[12:13], s[14:15], exec
	s_cselect_b32 s2, 2, s2
	v_cndmask_b32_e32 v36, v117, v37, vcc
	v_add_f32_e32 v36, 1.0, v36
	v_div_scale_f32 v37, s[12:13], v36, v36, 1.0
	v_rcp_f32_e32 v38, v37
	s_and_b64 s[12:13], s[16:17], exec
	s_cselect_b32 s2, 3, s2
	s_and_b64 s[12:13], s[18:19], exec
	s_cselect_b32 s2, 4, s2
	s_and_b64 s[12:13], s[20:21], exec
	v_fma_f32 v39, -v37, v38, 1.0
	s_cselect_b32 s2, 5, s2
	s_and_b64 s[12:13], s[24:25], exec
	v_fmac_f32_e32 v38, v39, v38
	v_div_scale_f32 v39, vcc, 1.0, v36, 1.0
	s_cselect_b32 s2, s2, 6
	s_and_b64 s[12:13], s[22:23], exec
	v_mul_f32_e32 v40, v39, v38
	s_cselect_b32 s2, 7, s2
	v_fma_f32 v41, -v37, v40, v39
	s_ashr_i32 s41, s40, 31
	v_fmac_f32_e32 v40, v41, v38
	s_lshl_b64 s[12:13], s[40:41], 2
	v_fma_f32 v37, -v37, v40, v39
	s_add_u32 s14, s33, s12
	v_div_fmas_f32 v37, v37, v38, v40
	s_addc_u32 s15, s35, s13
	v_div_fixup_f32 v36, v37, v36, 1.0
	s_add_u32 s12, s46, s12
	v_sub_f32_e32 v37, 1.0, v36
	s_addc_u32 s13, s47, s13
	global_store_dwordx2 v51, v[36:37], s[12:13]
	v_mbcnt_lo_u32_b32 v36, s44, 0
	v_mbcnt_hi_u32_b32 v36, s45, v36
	v_mov_b32_e32 v38, s61
	v_mov_b32_e32 v39, s2
	v_cmp_eq_u32_e32 vcc, 0, v36
	global_store_dwordx2 v51, v[38:39], s[14:15]
	s_and_saveexec_b64 s[12:13], vcc
	s_cbranch_execz .LBB0_1347
	s_lshl_b32 s14, s61, 2
	s_add_i32 s14, s14, 0
	s_add_i32 s14, s14, 0x10000
	s_bcnt1_i32_b64 s15, s[44:45]
	v_mov_b32_e32 v36, s14
	v_mov_b32_e32 v37, s15
	ds_add_u32 v36, v37
